# speedup vs baseline: 1.0036x; 1.0036x over previous
_Z11edge_kernelILi36ELb1EEvPKfS1_PKDF16_PKiS5_S1_S1_S1_S1_S1_PDF16_:
	s_load_dwordx8 s[4:11], s[0:1], 0x0
	s_load_dwordx8 s[12:19], s[0:1], 0x20
	s_load_dwordx4 s[20:23], s[0:1], 0x40
	s_load_dwordx2 s[24:25], s[0:1], 0x50
	v_readfirstlane_b32 s3, v0
	v_bfe_u32 v139, v0, 4, 2
	v_and_b32_e32 v140, 15, v0
	v_and_b32_e32 v142, 63, v0
	s_lshr_b32 s3, s3, 6
	s_lshl_b32 s2, s2, 1
	s_add_i32 s2, s2, s3
	v_lshlrev_b32_e32 v138, 8, v139
	v_lshl_or_b32 v138, v140, 4, v138
	v_lshlrev_b32_e32 v143, 4, v142
	v_lshl_or_b32 v141, v140, 2, v139
	v_lshlrev_b32_e32 v141, 2, v141
	v_mul_u32_u24_e32 v137, 0x900, v139
	v_lshl_or_b32 v137, v140, 4, v137
	v_mul_u32_u24_e32 v142, 36, v139
	s_mul_i32 s28, s2, 0x2400
	s_lshl_b32 s29, s2, 14
	s_lshl_b32 s30, s2, 2
	s_lshl_b32 s31, s2, 8
	s_lshl_b32 s33, s3, 10
	s_lshl_b32 s34, s3, 8
	s_addk_i32 s34, 0x4000
	s_waitcnt lgkmcnt(0)
	s_add_u32 s10, s10, s30
	s_addc_u32 s11, s11, 0
	s_add_u32 s12, s12, s30
	s_addc_u32 s13, s13, 0
	s_load_dword s35, s[10:11], 0x0
	s_load_dword s36, s[12:13], 0x0
	s_add_u32 s14, s14, s28
	s_addc_u32 s15, s15, 0
	global_load_dwordx4 v[0:3], v137, s[14:15] nt
	global_load_dwordx4 v[4:7], v137, s[14:15] offset:256 nt
	global_load_dwordx4 v[8:11], v137, s[14:15] offset:512 nt
	global_load_dwordx4 v[12:15], v137, s[14:15] offset:768 nt
	global_load_dwordx4 v[16:19], v137, s[14:15] offset:1024 nt
	global_load_dwordx4 v[20:23], v137, s[14:15] offset:1280 nt
	global_load_dwordx4 v[24:27], v137, s[14:15] offset:1536 nt
	global_load_dwordx4 v[28:31], v137, s[14:15] offset:1792 nt
	global_load_dwordx4 v[32:35], v137, s[14:15] offset:2048 nt
	s_add_u32 s22, s22, s33
	s_addc_u32 s23, s23, 0
	s_mov_b32 m0, s33
	s_add_u32 s18, s18, s29
	s_addc_u32 s19, s19, 0
	global_load_lds_dwordx4 v143, s[22:23]
	global_load_lds_dwordx4 v143, s[22:23] offset:2048
	s_add_u32 m0, m0, 0x1000
	s_add_u32 s22, s22, 0x1000
	s_addc_u32 s23, s23, 0
	global_load_lds_dwordx4 v143, s[22:23]
	global_load_lds_dwordx4 v143, s[22:23] offset:2048
	s_add_u32 m0, m0, 0x1000
	s_add_u32 s22, s22, 0x1000
	s_addc_u32 s23, s23, 0
	global_load_lds_dwordx4 v143, s[22:23]
	global_load_lds_dwordx4 v143, s[22:23] offset:2048
	s_add_u32 m0, m0, 0x1000
	s_add_u32 s22, s22, 0x1000
	s_addc_u32 s23, s23, 0
	global_load_lds_dwordx4 v143, s[22:23]
	global_load_lds_dwordx4 v143, s[22:23] offset:2048
	s_add_u32 s16, s16, s31
	s_addc_u32 s17, s17, 0
	s_add_u32 s20, s20, s31
	s_addc_u32 s21, s21, 0
	s_waitcnt lgkmcnt(0)
	s_lshl_b32 s36, s36, 7
	s_add_u32 s24, s24, s36
	s_addc_u32 s25, s25, 0
	s_lshl_b32 s37, s35, 7
	s_lshl_b32 s38, s35, 4
	s_add_u32 s4, s4, s37
	s_addc_u32 s5, s5, 0
	s_add_u32 s6, s6, s38
	s_addc_u32 s7, s7, 0
	v_mov_b32_e32 v157, 0
	v_mov_b32_e32 v156, v142
	v_lshl_add_u64 v[158:159], s[4:5], 0, v[156:157]
	v_lshl_add_u64 v[158:159], v[158:159], 0, 20
	v_cmp_eq_u32_e32 vcc, 3, v139
	s_nop 1
	v_mov_b32_e32 v154, s6
	v_mov_b32_e32 v155, s7
	v_cndmask_b32_e32 v158, v158, v154, vcc
	v_cndmask_b32_e32 v159, v159, v155, vcc
	global_load_dwordx4 v[144:147], v142, s[4:5] nt
	global_load_dword v148, v142, s[4:5] offset:16 nt
	global_load_dwordx4 v[150:153], v[158:159], off nt
	global_load_dword v136, v141, s[16:17] nt
	global_load_dword v128, v141, s[20:21] nt
	global_load_dwordx4 v[64:67], v138, s[18:19] nt
	global_load_dwordx4 v[68:71], v138, s[18:19] offset:1024 nt
	global_load_dwordx4 v[72:75], v138, s[18:19] offset:2048 nt
	global_load_dwordx4 v[76:79], v138, s[18:19] offset:3072 nt
	s_add_u32 s18, s18, 0x1000
	s_addc_u32 s19, s19, 0
	global_load_dwordx4 v[80:83], v138, s[18:19] nt
	global_load_dwordx4 v[84:87], v138, s[18:19] offset:1024 nt
	global_load_dwordx4 v[88:91], v138, s[18:19] offset:2048 nt
	global_load_dwordx4 v[92:95], v138, s[18:19] offset:3072 nt
	s_add_u32 s18, s18, 0x1000
	s_addc_u32 s19, s19, 0
	global_load_dwordx4 v[96:99], v138, s[18:19] nt
	global_load_dwordx4 v[100:103], v138, s[18:19] offset:1024 nt
	global_load_dwordx4 v[104:107], v138, s[18:19] offset:2048 nt
	global_load_dwordx4 v[108:111], v138, s[18:19] offset:3072 nt
	s_add_u32 s18, s18, 0x1000
	s_addc_u32 s19, s19, 0
	global_load_dwordx4 v[112:115], v138, s[18:19] nt
	global_load_dwordx4 v[116:119], v138, s[18:19] offset:1024 nt
	global_load_dwordx4 v[120:123], v138, s[18:19] offset:2048 nt
	global_load_dwordx4 v[124:127], v138, s[18:19] offset:3072 nt
	v_add_u32_e32 v142, s34, v141
	v_lshl_add_u32 v143, v139, 2, s34
	s_waitcnt vmcnt(18)
	s_barrier
	v_pk_mul_f32 v[160:161], v[144:145], v[0:1] op_sel_hi:[0,1]
	v_pk_mul_f32 v[162:163], v[144:145], v[2:3] op_sel_hi:[0,1]
	v_pk_mul_f32 v[164:165], v[144:145], v[4:5] op_sel:[1,0]
	v_pk_mul_f32 v[166:167], v[144:145], v[6:7] op_sel:[1,0]
	v_pk_fma_f32 v[160:161], v[146:147], v[8:9], v[160:161] op_sel_hi:[0,1,1]
	v_pk_fma_f32 v[162:163], v[146:147], v[10:11], v[162:163] op_sel_hi:[0,1,1]
	v_pk_fma_f32 v[164:165], v[146:147], v[12:13], v[164:165] op_sel:[1,0,0]
	v_pk_fma_f32 v[166:167], v[146:147], v[14:15], v[166:167] op_sel:[1,0,0]
	v_pk_fma_f32 v[160:161], v[148:149], v[16:17], v[160:161] op_sel_hi:[0,1,1]
	v_pk_fma_f32 v[162:163], v[148:149], v[18:19], v[162:163] op_sel_hi:[0,1,1]
	v_pk_fma_f32 v[164:165], v[150:151], v[20:21], v[164:165] op_sel_hi:[0,1,1]
	v_pk_fma_f32 v[166:167], v[150:151], v[22:23], v[166:167] op_sel_hi:[0,1,1]
	v_pk_fma_f32 v[160:161], v[150:151], v[24:25], v[160:161] op_sel:[1,0,0]
	v_pk_fma_f32 v[162:163], v[150:151], v[26:27], v[162:163] op_sel:[1,0,0]
	v_pk_fma_f32 v[164:165], v[152:153], v[28:29], v[164:165] op_sel_hi:[0,1,1]
	v_pk_fma_f32 v[166:167], v[152:153], v[30:31], v[166:167] op_sel_hi:[0,1,1]
	v_pk_fma_f32 v[160:161], v[152:153], v[32:33], v[160:161] op_sel:[1,0,0]
	v_pk_fma_f32 v[162:163], v[152:153], v[34:35], v[162:163] op_sel:[1,0,0]
	v_pk_add_f32 v[160:161], v[160:161], v[164:165]
	v_pk_add_f32 v[162:163], v[162:163], v[166:167]
	s_nop 1
	v_permlane16_swap_b32_e32 v160, v161
	v_permlane16_swap_b32_e32 v162, v163
	v_add_f32_e32 v160, v160, v161
	v_add_f32_e32 v162, v162, v163
	s_nop 1
	v_permlane32_swap_b32_e32 v160, v162
	v_add_f32_e32 v160, v160, v162
	s_waitcnt vmcnt(17)
	v_add_f32_e32 v160, v160, v136
	v_max_f32_e32 v160, 0, v160
	ds_write_b32 v142, v160
	ds_read2_b32 v[144:145], v143 offset0:0 offset1:4
	ds_read2_b32 v[146:147], v143 offset0:8 offset1:12
	ds_read2_b32 v[148:149], v143 offset0:16 offset1:20
	ds_read2_b32 v[150:151], v143 offset0:24 offset1:28
	ds_read2_b32 v[152:153], v143 offset0:32 offset1:36
	ds_read2_b32 v[154:155], v143 offset0:40 offset1:44
	ds_read2_b32 v[156:157], v143 offset0:48 offset1:52
	ds_read2_b32 v[158:159], v143 offset0:56 offset1:60
	ds_read_b128 v[0:3], v138
	ds_read_b128 v[4:7], v138 offset:1024
	ds_read_b128 v[8:11], v138 offset:2048
	ds_read_b128 v[12:15], v138 offset:3072
	ds_read_b128 v[16:19], v138 offset:4096
	ds_read_b128 v[20:23], v138 offset:5120
	s_waitcnt lgkmcnt(6)
	s_waitcnt vmcnt(12)
	v_pk_mul_f32 v[160:161], v[144:145], v[64:65] op_sel_hi:[0,1]
	v_pk_mul_f32 v[162:163], v[144:145], v[66:67] op_sel_hi:[0,1]
	v_pk_mul_f32 v[164:165], v[144:145], v[68:69] op_sel:[1,0]
	v_pk_mul_f32 v[166:167], v[144:145], v[70:71] op_sel:[1,0]
	v_pk_fma_f32 v[160:161], v[146:147], v[72:73], v[160:161] op_sel_hi:[0,1,1]
	v_pk_fma_f32 v[162:163], v[146:147], v[74:75], v[162:163] op_sel_hi:[0,1,1]
	v_pk_fma_f32 v[164:165], v[146:147], v[76:77], v[164:165] op_sel:[1,0,0]
	v_pk_fma_f32 v[166:167], v[146:147], v[78:79], v[166:167] op_sel:[1,0,0]
	ds_read_b128 v[24:27], v138 offset:6144
	ds_read_b128 v[28:31], v138 offset:7168
	ds_read_b128 v[32:35], v138 offset:8192
	ds_read_b128 v[36:39], v138 offset:9216
	ds_read_b128 v[40:43], v138 offset:10240
	ds_read_b128 v[44:47], v138 offset:11264
	s_waitcnt vmcnt(8)
	v_pk_fma_f32 v[160:161], v[148:149], v[80:81], v[160:161] op_sel_hi:[0,1,1]
	v_pk_fma_f32 v[162:163], v[148:149], v[82:83], v[162:163] op_sel_hi:[0,1,1]
	v_pk_fma_f32 v[164:165], v[148:149], v[84:85], v[164:165] op_sel:[1,0,0]
	v_pk_fma_f32 v[166:167], v[148:149], v[86:87], v[166:167] op_sel:[1,0,0]
	v_pk_fma_f32 v[160:161], v[150:151], v[88:89], v[160:161] op_sel_hi:[0,1,1]
	v_pk_fma_f32 v[162:163], v[150:151], v[90:91], v[162:163] op_sel_hi:[0,1,1]
	v_pk_fma_f32 v[164:165], v[150:151], v[92:93], v[164:165] op_sel:[1,0,0]
	v_pk_fma_f32 v[166:167], v[150:151], v[94:95], v[166:167] op_sel:[1,0,0]
	s_waitcnt lgkmcnt(4)
	ds_read_b128 v[48:51], v138 offset:12288
	ds_read_b128 v[52:55], v138 offset:13312
	ds_read_b128 v[56:59], v138 offset:14336
	ds_read_b128 v[60:63], v138 offset:15360
	s_waitcnt vmcnt(4)
	v_pk_fma_f32 v[160:161], v[152:153], v[96:97], v[160:161] op_sel_hi:[0,1,1]
	v_pk_fma_f32 v[162:163], v[152:153], v[98:99], v[162:163] op_sel_hi:[0,1,1]
	v_pk_fma_f32 v[164:165], v[152:153], v[100:101], v[164:165] op_sel:[1,0,0]
	v_pk_fma_f32 v[166:167], v[152:153], v[102:103], v[166:167] op_sel:[1,0,0]
	v_pk_fma_f32 v[160:161], v[154:155], v[104:105], v[160:161] op_sel_hi:[0,1,1]
	v_pk_fma_f32 v[162:163], v[154:155], v[106:107], v[162:163] op_sel_hi:[0,1,1]
	v_pk_fma_f32 v[164:165], v[154:155], v[108:109], v[164:165] op_sel:[1,0,0]
	v_pk_fma_f32 v[166:167], v[154:155], v[110:111], v[166:167] op_sel:[1,0,0]
	s_waitcnt vmcnt(0)
	v_pk_fma_f32 v[160:161], v[156:157], v[112:113], v[160:161] op_sel_hi:[0,1,1]
	v_pk_fma_f32 v[162:163], v[156:157], v[114:115], v[162:163] op_sel_hi:[0,1,1]
	v_pk_fma_f32 v[164:165], v[156:157], v[116:117], v[164:165] op_sel:[1,0,0]
	v_pk_fma_f32 v[166:167], v[156:157], v[118:119], v[166:167] op_sel:[1,0,0]
	v_pk_fma_f32 v[160:161], v[158:159], v[120:121], v[160:161] op_sel_hi:[0,1,1]
	v_pk_fma_f32 v[162:163], v[158:159], v[122:123], v[162:163] op_sel_hi:[0,1,1]
	v_pk_fma_f32 v[164:165], v[158:159], v[124:125], v[164:165] op_sel:[1,0,0]
	v_pk_fma_f32 v[166:167], v[158:159], v[126:127], v[166:167] op_sel:[1,0,0]
	v_pk_add_f32 v[160:161], v[160:161], v[164:165]
	v_pk_add_f32 v[162:163], v[162:163], v[166:167]
	s_nop 1
	v_permlane16_swap_b32_e32 v160, v161
	v_permlane16_swap_b32_e32 v162, v163
	v_add_f32_e32 v160, v160, v161
	v_add_f32_e32 v162, v162, v163
	s_nop 1
	v_permlane32_swap_b32_e32 v160, v162
	v_add_f32_e32 v160, v160, v162
	v_add_f32_e32 v160, v160, v128
	s_waitcnt lgkmcnt(0)
	ds_write_b32 v142, v160
	ds_read2_b32 v[144:145], v143 offset0:0 offset1:4
	ds_read2_b32 v[146:147], v143 offset0:8 offset1:12
	ds_read2_b32 v[148:149], v143 offset0:16 offset1:20
	ds_read2_b32 v[150:151], v143 offset0:24 offset1:28
	ds_read2_b32 v[152:153], v143 offset0:32 offset1:36
	ds_read2_b32 v[154:155], v143 offset0:40 offset1:44
	ds_read2_b32 v[156:157], v143 offset0:48 offset1:52
	ds_read2_b32 v[158:159], v143 offset0:56 offset1:60
	v_lshlrev_b32_e32 v136, 3, v140
	v_lshl_or_b32 v136, v139, 2, v136
	v_cmp_gt_u32_e32 vcc, 2, v139
	s_waitcnt lgkmcnt(0)
	v_pk_mul_f32 v[160:161], v[144:145], v[0:1] op_sel_hi:[0,1]
	v_pk_mul_f32 v[162:163], v[144:145], v[2:3] op_sel_hi:[0,1]
	v_pk_mul_f32 v[164:165], v[144:145], v[4:5] op_sel:[1,0]
	v_pk_mul_f32 v[166:167], v[144:145], v[6:7] op_sel:[1,0]
	v_pk_fma_f32 v[160:161], v[146:147], v[8:9], v[160:161] op_sel_hi:[0,1,1]
	v_pk_fma_f32 v[162:163], v[146:147], v[10:11], v[162:163] op_sel_hi:[0,1,1]
	v_pk_fma_f32 v[164:165], v[146:147], v[12:13], v[164:165] op_sel:[1,0,0]
	v_pk_fma_f32 v[166:167], v[146:147], v[14:15], v[166:167] op_sel:[1,0,0]
	v_pk_fma_f32 v[160:161], v[148:149], v[16:17], v[160:161] op_sel_hi:[0,1,1]
	v_pk_fma_f32 v[162:163], v[148:149], v[18:19], v[162:163] op_sel_hi:[0,1,1]
	v_pk_fma_f32 v[164:165], v[148:149], v[20:21], v[164:165] op_sel:[1,0,0]
	v_pk_fma_f32 v[166:167], v[148:149], v[22:23], v[166:167] op_sel:[1,0,0]
	v_pk_fma_f32 v[160:161], v[150:151], v[24:25], v[160:161] op_sel_hi:[0,1,1]
	v_pk_fma_f32 v[162:163], v[150:151], v[26:27], v[162:163] op_sel_hi:[0,1,1]
	v_pk_fma_f32 v[164:165], v[150:151], v[28:29], v[164:165] op_sel:[1,0,0]
	v_pk_fma_f32 v[166:167], v[150:151], v[30:31], v[166:167] op_sel:[1,0,0]
	v_pk_fma_f32 v[160:161], v[152:153], v[32:33], v[160:161] op_sel_hi:[0,1,1]
	v_pk_fma_f32 v[162:163], v[152:153], v[34:35], v[162:163] op_sel_hi:[0,1,1]
	v_pk_fma_f32 v[164:165], v[152:153], v[36:37], v[164:165] op_sel:[1,0,0]
	v_pk_fma_f32 v[166:167], v[152:153], v[38:39], v[166:167] op_sel:[1,0,0]
	v_pk_fma_f32 v[160:161], v[154:155], v[40:41], v[160:161] op_sel_hi:[0,1,1]
	v_pk_fma_f32 v[162:163], v[154:155], v[42:43], v[162:163] op_sel_hi:[0,1,1]
	v_pk_fma_f32 v[164:165], v[154:155], v[44:45], v[164:165] op_sel:[1,0,0]
	v_pk_fma_f32 v[166:167], v[154:155], v[46:47], v[166:167] op_sel:[1,0,0]
	v_pk_fma_f32 v[160:161], v[156:157], v[48:49], v[160:161] op_sel_hi:[0,1,1]
	v_pk_fma_f32 v[162:163], v[156:157], v[50:51], v[162:163] op_sel_hi:[0,1,1]
	v_pk_fma_f32 v[164:165], v[156:157], v[52:53], v[164:165] op_sel:[1,0,0]
	v_pk_fma_f32 v[166:167], v[156:157], v[54:55], v[166:167] op_sel:[1,0,0]
	v_pk_fma_f32 v[160:161], v[158:159], v[56:57], v[160:161] op_sel_hi:[0,1,1]
	v_pk_fma_f32 v[162:163], v[158:159], v[58:59], v[162:163] op_sel_hi:[0,1,1]
	v_pk_fma_f32 v[164:165], v[158:159], v[60:61], v[164:165] op_sel:[1,0,0]
	v_pk_fma_f32 v[166:167], v[158:159], v[62:63], v[166:167] op_sel:[1,0,0]
	v_pk_add_f32 v[160:161], v[160:161], v[164:165]
	v_pk_add_f32 v[162:163], v[162:163], v[166:167]
	s_nop 1
	v_permlane16_swap_b32_e32 v160, v162
	v_permlane16_swap_b32_e32 v161, v163
	v_add_f32_e32 v160, v160, v162
	v_add_f32_e32 v161, v161, v163
	v_mov_b32_e32 v144, v160
	v_mov_b32_e32 v145, v161
	s_nop 1
	v_permlane32_swap_b32_e32 v160, v144
	v_permlane32_swap_b32_e32 v161, v145
	v_add_f32_e32 v160, v160, v144
	v_add_f32_e32 v161, v161, v145
	v_cvt_pk_f16_f32 v137, v160, v161
	s_and_saveexec_b64 s[4:5], vcc
	global_atomic_pk_add_f16 v136, v137, s[24:25]
	s_endpgm
	.p2align	8

_Z11edge_kernelILi64ELb0EEvPKfS1_PKDF16_PKiS5_S1_S1_S1_S1_S1_PDF16_:
	s_load_dwordx16 s[4:19], s[0:1], 0x10
	s_load_dwordx2 s[20:21], s[0:1], 0x50
	v_readfirstlane_b32 s3, v0
	v_bfe_u32 v139, v0, 4, 2
	v_and_b32_e32 v140, 15, v0
	v_and_b32_e32 v142, 63, v0
	s_lshr_b32 s3, s3, 6
	s_lshl_b32 s2, s2, 1
	s_add_i32 s2, s2, s3
	v_lshlrev_b32_e32 v138, 8, v139
	v_lshl_or_b32 v138, v140, 4, v138
	v_lshlrev_b32_e32 v143, 4, v142
	v_lshl_or_b32 v141, v140, 2, v139
	v_lshlrev_b32_e32 v141, 2, v141
	v_lshlrev_b32_e32 v142, 5, v139
	v_lshlrev_b32_e32 v137, 12, v139
	v_lshl_or_b32 v137, v140, 4, v137
	s_lshl_b32 s28, s2, 14
	s_lshl_b32 s29, s2, 14
	s_lshl_b32 s30, s2, 2
	s_lshl_b32 s31, s2, 8
	s_lshl_b32 s33, s3, 10
	s_lshl_b32 s34, s3, 8
	s_addk_i32 s34, 0x4000
	s_waitcnt lgkmcnt(0)
	s_add_u32 s6, s6, s30
	s_addc_u32 s7, s7, 0
	s_add_u32 s8, s8, s30
	s_addc_u32 s9, s9, 0
	s_load_dword s35, s[6:7], 0x0
	s_load_dword s36, s[8:9], 0x0
	s_add_u32 s10, s10, s28
	s_addc_u32 s11, s11, 0
	global_load_dwordx4 v[0:3], v137, s[10:11] nt
	global_load_dwordx4 v[4:7], v137, s[10:11] offset:256 nt
	global_load_dwordx4 v[8:11], v137, s[10:11] offset:512 nt
	global_load_dwordx4 v[12:15], v137, s[10:11] offset:768 nt
	global_load_dwordx4 v[16:19], v137, s[10:11] offset:1024 nt
	global_load_dwordx4 v[20:23], v137, s[10:11] offset:1280 nt
	global_load_dwordx4 v[24:27], v137, s[10:11] offset:1536 nt
	global_load_dwordx4 v[28:31], v137, s[10:11] offset:1792 nt
	global_load_dwordx4 v[32:35], v137, s[10:11] offset:2048 nt
	global_load_dwordx4 v[36:39], v137, s[10:11] offset:2304 nt
	global_load_dwordx4 v[40:43], v137, s[10:11] offset:2560 nt
	global_load_dwordx4 v[44:47], v137, s[10:11] offset:2816 nt
	global_load_dwordx4 v[48:51], v137, s[10:11] offset:3072 nt
	global_load_dwordx4 v[52:55], v137, s[10:11] offset:3328 nt
	global_load_dwordx4 v[56:59], v137, s[10:11] offset:3584 nt
	global_load_dwordx4 v[60:63], v137, s[10:11] offset:3840 nt
	s_add_u32 s18, s18, s33
	s_addc_u32 s19, s19, 0
	s_mov_b32 m0, s33
	s_add_u32 s14, s14, s29
	s_addc_u32 s15, s15, 0
	global_load_lds_dwordx4 v143, s[18:19]
	global_load_lds_dwordx4 v143, s[18:19] offset:2048
	s_add_u32 m0, m0, 0x1000
	s_add_u32 s18, s18, 0x1000
	s_addc_u32 s19, s19, 0
	global_load_lds_dwordx4 v143, s[18:19]
	global_load_lds_dwordx4 v143, s[18:19] offset:2048
	s_add_u32 m0, m0, 0x1000
	s_add_u32 s18, s18, 0x1000
	s_addc_u32 s19, s19, 0
	global_load_lds_dwordx4 v143, s[18:19]
	global_load_lds_dwordx4 v143, s[18:19] offset:2048
	s_add_u32 m0, m0, 0x1000
	s_add_u32 s18, s18, 0x1000
	s_addc_u32 s19, s19, 0
	global_load_lds_dwordx4 v143, s[18:19]
	global_load_lds_dwordx4 v143, s[18:19] offset:2048
	s_add_u32 s12, s12, s31
	s_addc_u32 s13, s13, 0
	s_add_u32 s16, s16, s31
	s_addc_u32 s17, s17, 0
	s_waitcnt lgkmcnt(0)
	s_lshl_b32 s36, s36, 7
	s_add_u32 s20, s20, s36
	s_addc_u32 s21, s21, 0
	s_lshl_b32 s37, s35, 7
	s_add_u32 s4, s4, s37
	s_addc_u32 s5, s5, 0
	global_load_dwordx4 v[128:131], v142, s[4:5] nt
	global_load_dwordx4 v[132:135], v142, s[4:5] offset:16 nt
	global_load_dword v136, v141, s[12:13] nt
	global_load_dword v137, v141, s[16:17] nt
	global_load_dwordx4 v[64:67], v138, s[14:15] nt
	global_load_dwordx4 v[68:71], v138, s[14:15] offset:1024 nt
	global_load_dwordx4 v[72:75], v138, s[14:15] offset:2048 nt
	global_load_dwordx4 v[76:79], v138, s[14:15] offset:3072 nt
	s_add_u32 s14, s14, 0x1000
	s_addc_u32 s15, s15, 0
	global_load_dwordx4 v[80:83], v138, s[14:15] nt
	global_load_dwordx4 v[84:87], v138, s[14:15] offset:1024 nt
	global_load_dwordx4 v[88:91], v138, s[14:15] offset:2048 nt
	global_load_dwordx4 v[92:95], v138, s[14:15] offset:3072 nt
	s_add_u32 s14, s14, 0x1000
	s_addc_u32 s15, s15, 0
	global_load_dwordx4 v[96:99], v138, s[14:15] nt
	global_load_dwordx4 v[100:103], v138, s[14:15] offset:1024 nt
	global_load_dwordx4 v[104:107], v138, s[14:15] offset:2048 nt
	global_load_dwordx4 v[108:111], v138, s[14:15] offset:3072 nt
	s_add_u32 s14, s14, 0x1000
	s_addc_u32 s15, s15, 0
	global_load_dwordx4 v[112:115], v138, s[14:15] nt
	global_load_dwordx4 v[116:119], v138, s[14:15] offset:1024 nt
	global_load_dwordx4 v[120:123], v138, s[14:15] offset:2048 nt
	global_load_dwordx4 v[124:127], v138, s[14:15] offset:3072 nt
	v_add_u32_e32 v142, s34, v141
	v_lshl_add_u32 v143, v139, 2, s34
	s_waitcnt vmcnt(18)
	s_barrier
	v_cvt_f32_f16_e32 v144, v128
	v_cvt_f32_f16_sdwa v145, v128 dst_sel:DWORD dst_unused:UNUSED_PAD src0_sel:WORD_1
	v_cvt_f32_f16_e32 v146, v129
	v_cvt_f32_f16_sdwa v147, v129 dst_sel:DWORD dst_unused:UNUSED_PAD src0_sel:WORD_1
	v_cvt_f32_f16_e32 v148, v130
	v_cvt_f32_f16_sdwa v149, v130 dst_sel:DWORD dst_unused:UNUSED_PAD src0_sel:WORD_1
	v_cvt_f32_f16_e32 v150, v131
	v_cvt_f32_f16_sdwa v151, v131 dst_sel:DWORD dst_unused:UNUSED_PAD src0_sel:WORD_1
	v_cvt_f32_f16_e32 v152, v132
	v_cvt_f32_f16_sdwa v153, v132 dst_sel:DWORD dst_unused:UNUSED_PAD src0_sel:WORD_1
	v_cvt_f32_f16_e32 v154, v133
	v_cvt_f32_f16_sdwa v155, v133 dst_sel:DWORD dst_unused:UNUSED_PAD src0_sel:WORD_1
	v_cvt_f32_f16_e32 v156, v134
	v_cvt_f32_f16_sdwa v157, v134 dst_sel:DWORD dst_unused:UNUSED_PAD src0_sel:WORD_1
	v_cvt_f32_f16_e32 v158, v135
	v_cvt_f32_f16_sdwa v159, v135 dst_sel:DWORD dst_unused:UNUSED_PAD src0_sel:WORD_1
	v_max_f32_e32 v144, 0, v144
	v_max_f32_e32 v145, 0, v145
	v_max_f32_e32 v146, 0, v146
	v_max_f32_e32 v147, 0, v147
	v_max_f32_e32 v148, 0, v148
	v_max_f32_e32 v149, 0, v149
	v_max_f32_e32 v150, 0, v150
	v_max_f32_e32 v151, 0, v151
	v_max_f32_e32 v152, 0, v152
	v_max_f32_e32 v153, 0, v153
	v_max_f32_e32 v154, 0, v154
	v_max_f32_e32 v155, 0, v155
	v_max_f32_e32 v156, 0, v156
	v_max_f32_e32 v157, 0, v157
	v_max_f32_e32 v158, 0, v158
	v_max_f32_e32 v159, 0, v159
	v_pk_mul_f32 v[160:161], v[144:145], v[0:1] op_sel_hi:[0,1]
	v_pk_mul_f32 v[162:163], v[144:145], v[2:3] op_sel_hi:[0,1]
	v_pk_mul_f32 v[164:165], v[144:145], v[4:5] op_sel:[1,0]
	v_pk_mul_f32 v[166:167], v[144:145], v[6:7] op_sel:[1,0]
	v_pk_fma_f32 v[160:161], v[146:147], v[8:9], v[160:161] op_sel_hi:[0,1,1]
	v_pk_fma_f32 v[162:163], v[146:147], v[10:11], v[162:163] op_sel_hi:[0,1,1]
	v_pk_fma_f32 v[164:165], v[146:147], v[12:13], v[164:165] op_sel:[1,0,0]
	v_pk_fma_f32 v[166:167], v[146:147], v[14:15], v[166:167] op_sel:[1,0,0]
	v_pk_fma_f32 v[160:161], v[148:149], v[16:17], v[160:161] op_sel_hi:[0,1,1]
	v_pk_fma_f32 v[162:163], v[148:149], v[18:19], v[162:163] op_sel_hi:[0,1,1]
	v_pk_fma_f32 v[164:165], v[148:149], v[20:21], v[164:165] op_sel:[1,0,0]
	v_pk_fma_f32 v[166:167], v[148:149], v[22:23], v[166:167] op_sel:[1,0,0]
	v_pk_fma_f32 v[160:161], v[150:151], v[24:25], v[160:161] op_sel_hi:[0,1,1]
	v_pk_fma_f32 v[162:163], v[150:151], v[26:27], v[162:163] op_sel_hi:[0,1,1]
	v_pk_fma_f32 v[164:165], v[150:151], v[28:29], v[164:165] op_sel:[1,0,0]
	v_pk_fma_f32 v[166:167], v[150:151], v[30:31], v[166:167] op_sel:[1,0,0]
	v_pk_fma_f32 v[160:161], v[152:153], v[32:33], v[160:161] op_sel_hi:[0,1,1]
	v_pk_fma_f32 v[162:163], v[152:153], v[34:35], v[162:163] op_sel_hi:[0,1,1]
	v_pk_fma_f32 v[164:165], v[152:153], v[36:37], v[164:165] op_sel:[1,0,0]
	v_pk_fma_f32 v[166:167], v[152:153], v[38:39], v[166:167] op_sel:[1,0,0]
	v_pk_fma_f32 v[160:161], v[154:155], v[40:41], v[160:161] op_sel_hi:[0,1,1]
	v_pk_fma_f32 v[162:163], v[154:155], v[42:43], v[162:163] op_sel_hi:[0,1,1]
	v_pk_fma_f32 v[164:165], v[154:155], v[44:45], v[164:165] op_sel:[1,0,0]
	v_pk_fma_f32 v[166:167], v[154:155], v[46:47], v[166:167] op_sel:[1,0,0]
	v_pk_fma_f32 v[160:161], v[156:157], v[48:49], v[160:161] op_sel_hi:[0,1,1]
	v_pk_fma_f32 v[162:163], v[156:157], v[50:51], v[162:163] op_sel_hi:[0,1,1]
	v_pk_fma_f32 v[164:165], v[156:157], v[52:53], v[164:165] op_sel:[1,0,0]
	v_pk_fma_f32 v[166:167], v[156:157], v[54:55], v[166:167] op_sel:[1,0,0]
	v_pk_fma_f32 v[160:161], v[158:159], v[56:57], v[160:161] op_sel_hi:[0,1,1]
	v_pk_fma_f32 v[162:163], v[158:159], v[58:59], v[162:163] op_sel_hi:[0,1,1]
	v_pk_fma_f32 v[164:165], v[158:159], v[60:61], v[164:165] op_sel:[1,0,0]
	v_pk_fma_f32 v[166:167], v[158:159], v[62:63], v[166:167] op_sel:[1,0,0]
	v_pk_add_f32 v[160:161], v[160:161], v[164:165]
	v_pk_add_f32 v[162:163], v[162:163], v[166:167]
	s_nop 1
	v_permlane16_swap_b32_e32 v160, v161
	v_permlane16_swap_b32_e32 v162, v163
	v_add_f32_e32 v160, v160, v161
	v_add_f32_e32 v162, v162, v163
	s_nop 1
	v_permlane32_swap_b32_e32 v160, v162
	v_add_f32_e32 v160, v160, v162
	s_waitcnt vmcnt(17)
	v_add_f32_e32 v160, v160, v136
	v_max_f32_e32 v160, 0, v160
	ds_write_b32 v142, v160
	ds_read2_b32 v[144:145], v143 offset0:0 offset1:4
	ds_read2_b32 v[146:147], v143 offset0:8 offset1:12
	ds_read2_b32 v[148:149], v143 offset0:16 offset1:20
	ds_read2_b32 v[150:151], v143 offset0:24 offset1:28
	ds_read2_b32 v[152:153], v143 offset0:32 offset1:36
	ds_read2_b32 v[154:155], v143 offset0:40 offset1:44
	ds_read2_b32 v[156:157], v143 offset0:48 offset1:52
	ds_read2_b32 v[158:159], v143 offset0:56 offset1:60
	ds_read_b128 v[0:3], v138
	ds_read_b128 v[4:7], v138 offset:1024
	ds_read_b128 v[8:11], v138 offset:2048
	ds_read_b128 v[12:15], v138 offset:3072
	ds_read_b128 v[16:19], v138 offset:4096
	ds_read_b128 v[20:23], v138 offset:5120
	s_waitcnt lgkmcnt(6)
	s_waitcnt vmcnt(12)
	v_pk_mul_f32 v[160:161], v[144:145], v[64:65] op_sel_hi:[0,1]
	v_pk_mul_f32 v[162:163], v[144:145], v[66:67] op_sel_hi:[0,1]
	v_pk_mul_f32 v[164:165], v[144:145], v[68:69] op_sel:[1,0]
	v_pk_mul_f32 v[166:167], v[144:145], v[70:71] op_sel:[1,0]
	v_pk_fma_f32 v[160:161], v[146:147], v[72:73], v[160:161] op_sel_hi:[0,1,1]
	v_pk_fma_f32 v[162:163], v[146:147], v[74:75], v[162:163] op_sel_hi:[0,1,1]
	v_pk_fma_f32 v[164:165], v[146:147], v[76:77], v[164:165] op_sel:[1,0,0]
	v_pk_fma_f32 v[166:167], v[146:147], v[78:79], v[166:167] op_sel:[1,0,0]
	ds_read_b128 v[24:27], v138 offset:6144
	ds_read_b128 v[28:31], v138 offset:7168
	ds_read_b128 v[32:35], v138 offset:8192
	ds_read_b128 v[36:39], v138 offset:9216
	ds_read_b128 v[40:43], v138 offset:10240
	ds_read_b128 v[44:47], v138 offset:11264
	s_waitcnt vmcnt(8)
	v_pk_fma_f32 v[160:161], v[148:149], v[80:81], v[160:161] op_sel_hi:[0,1,1]
	v_pk_fma_f32 v[162:163], v[148:149], v[82:83], v[162:163] op_sel_hi:[0,1,1]
	v_pk_fma_f32 v[164:165], v[148:149], v[84:85], v[164:165] op_sel:[1,0,0]
	v_pk_fma_f32 v[166:167], v[148:149], v[86:87], v[166:167] op_sel:[1,0,0]
	v_pk_fma_f32 v[160:161], v[150:151], v[88:89], v[160:161] op_sel_hi:[0,1,1]
	v_pk_fma_f32 v[162:163], v[150:151], v[90:91], v[162:163] op_sel_hi:[0,1,1]
	v_pk_fma_f32 v[164:165], v[150:151], v[92:93], v[164:165] op_sel:[1,0,0]
	v_pk_fma_f32 v[166:167], v[150:151], v[94:95], v[166:167] op_sel:[1,0,0]
	s_waitcnt lgkmcnt(4)
	ds_read_b128 v[48:51], v138 offset:12288
	ds_read_b128 v[52:55], v138 offset:13312
	ds_read_b128 v[56:59], v138 offset:14336
	ds_read_b128 v[60:63], v138 offset:15360
	s_waitcnt vmcnt(4)
	v_pk_fma_f32 v[160:161], v[152:153], v[96:97], v[160:161] op_sel_hi:[0,1,1]
	v_pk_fma_f32 v[162:163], v[152:153], v[98:99], v[162:163] op_sel_hi:[0,1,1]
	v_pk_fma_f32 v[164:165], v[152:153], v[100:101], v[164:165] op_sel:[1,0,0]
	v_pk_fma_f32 v[166:167], v[152:153], v[102:103], v[166:167] op_sel:[1,0,0]
	v_pk_fma_f32 v[160:161], v[154:155], v[104:105], v[160:161] op_sel_hi:[0,1,1]
	v_pk_fma_f32 v[162:163], v[154:155], v[106:107], v[162:163] op_sel_hi:[0,1,1]
	v_pk_fma_f32 v[164:165], v[154:155], v[108:109], v[164:165] op_sel:[1,0,0]
	v_pk_fma_f32 v[166:167], v[154:155], v[110:111], v[166:167] op_sel:[1,0,0]
	s_waitcnt vmcnt(0)
	v_pk_fma_f32 v[160:161], v[156:157], v[112:113], v[160:161] op_sel_hi:[0,1,1]
	v_pk_fma_f32 v[162:163], v[156:157], v[114:115], v[162:163] op_sel_hi:[0,1,1]
	v_pk_fma_f32 v[164:165], v[156:157], v[116:117], v[164:165] op_sel:[1,0,0]
	v_pk_fma_f32 v[166:167], v[156:157], v[118:119], v[166:167] op_sel:[1,0,0]
	v_pk_fma_f32 v[160:161], v[158:159], v[120:121], v[160:161] op_sel_hi:[0,1,1]
	v_pk_fma_f32 v[162:163], v[158:159], v[122:123], v[162:163] op_sel_hi:[0,1,1]
	v_pk_fma_f32 v[164:165], v[158:159], v[124:125], v[164:165] op_sel:[1,0,0]
	v_pk_fma_f32 v[166:167], v[158:159], v[126:127], v[166:167] op_sel:[1,0,0]
	v_pk_add_f32 v[160:161], v[160:161], v[164:165]
	v_pk_add_f32 v[162:163], v[162:163], v[166:167]
	s_nop 1
	v_permlane16_swap_b32_e32 v160, v161
	v_permlane16_swap_b32_e32 v162, v163
	v_add_f32_e32 v160, v160, v161
	v_add_f32_e32 v162, v162, v163
	s_nop 1
	v_permlane32_swap_b32_e32 v160, v162
	v_add_f32_e32 v160, v160, v162
	v_add_f32_e32 v160, v160, v137
	s_waitcnt lgkmcnt(0)
	ds_write_b32 v142, v160
	ds_read2_b32 v[144:145], v143 offset0:0 offset1:4
	ds_read2_b32 v[146:147], v143 offset0:8 offset1:12
	ds_read2_b32 v[148:149], v143 offset0:16 offset1:20
	ds_read2_b32 v[150:151], v143 offset0:24 offset1:28
	ds_read2_b32 v[152:153], v143 offset0:32 offset1:36
	ds_read2_b32 v[154:155], v143 offset0:40 offset1:44
	ds_read2_b32 v[156:157], v143 offset0:48 offset1:52
	ds_read2_b32 v[158:159], v143 offset0:56 offset1:60
	v_lshlrev_b32_e32 v136, 3, v140
	v_lshl_or_b32 v136, v139, 2, v136
	v_cmp_gt_u32_e32 vcc, 2, v139
	s_waitcnt lgkmcnt(0)
	v_pk_mul_f32 v[160:161], v[144:145], v[0:1] op_sel_hi:[0,1]
	v_pk_mul_f32 v[162:163], v[144:145], v[2:3] op_sel_hi:[0,1]
	v_pk_mul_f32 v[164:165], v[144:145], v[4:5] op_sel:[1,0]
	v_pk_mul_f32 v[166:167], v[144:145], v[6:7] op_sel:[1,0]
	v_pk_fma_f32 v[160:161], v[146:147], v[8:9], v[160:161] op_sel_hi:[0,1,1]
	v_pk_fma_f32 v[162:163], v[146:147], v[10:11], v[162:163] op_sel_hi:[0,1,1]
	v_pk_fma_f32 v[164:165], v[146:147], v[12:13], v[164:165] op_sel:[1,0,0]
	v_pk_fma_f32 v[166:167], v[146:147], v[14:15], v[166:167] op_sel:[1,0,0]
	v_pk_fma_f32 v[160:161], v[148:149], v[16:17], v[160:161] op_sel_hi:[0,1,1]
	v_pk_fma_f32 v[162:163], v[148:149], v[18:19], v[162:163] op_sel_hi:[0,1,1]
	v_pk_fma_f32 v[164:165], v[148:149], v[20:21], v[164:165] op_sel:[1,0,0]
	v_pk_fma_f32 v[166:167], v[148:149], v[22:23], v[166:167] op_sel:[1,0,0]
	v_pk_fma_f32 v[160:161], v[150:151], v[24:25], v[160:161] op_sel_hi:[0,1,1]
	v_pk_fma_f32 v[162:163], v[150:151], v[26:27], v[162:163] op_sel_hi:[0,1,1]
	v_pk_fma_f32 v[164:165], v[150:151], v[28:29], v[164:165] op_sel:[1,0,0]
	v_pk_fma_f32 v[166:167], v[150:151], v[30:31], v[166:167] op_sel:[1,0,0]
	v_pk_fma_f32 v[160:161], v[152:153], v[32:33], v[160:161] op_sel_hi:[0,1,1]
	v_pk_fma_f32 v[162:163], v[152:153], v[34:35], v[162:163] op_sel_hi:[0,1,1]
	v_pk_fma_f32 v[164:165], v[152:153], v[36:37], v[164:165] op_sel:[1,0,0]
	v_pk_fma_f32 v[166:167], v[152:153], v[38:39], v[166:167] op_sel:[1,0,0]
	v_pk_fma_f32 v[160:161], v[154:155], v[40:41], v[160:161] op_sel_hi:[0,1,1]
	v_pk_fma_f32 v[162:163], v[154:155], v[42:43], v[162:163] op_sel_hi:[0,1,1]
	v_pk_fma_f32 v[164:165], v[154:155], v[44:45], v[164:165] op_sel:[1,0,0]
	v_pk_fma_f32 v[166:167], v[154:155], v[46:47], v[166:167] op_sel:[1,0,0]
	v_pk_fma_f32 v[160:161], v[156:157], v[48:49], v[160:161] op_sel_hi:[0,1,1]
	v_pk_fma_f32 v[162:163], v[156:157], v[50:51], v[162:163] op_sel_hi:[0,1,1]
	v_pk_fma_f32 v[164:165], v[156:157], v[52:53], v[164:165] op_sel:[1,0,0]
	v_pk_fma_f32 v[166:167], v[156:157], v[54:55], v[166:167] op_sel:[1,0,0]
	v_pk_fma_f32 v[160:161], v[158:159], v[56:57], v[160:161] op_sel_hi:[0,1,1]
	v_pk_fma_f32 v[162:163], v[158:159], v[58:59], v[162:163] op_sel_hi:[0,1,1]
	v_pk_fma_f32 v[164:165], v[158:159], v[60:61], v[164:165] op_sel:[1,0,0]
	v_pk_fma_f32 v[166:167], v[158:159], v[62:63], v[166:167] op_sel:[1,0,0]
	v_pk_add_f32 v[160:161], v[160:161], v[164:165]
	v_pk_add_f32 v[162:163], v[162:163], v[166:167]
	s_nop 1
	v_permlane16_swap_b32_e32 v160, v162
	v_permlane16_swap_b32_e32 v161, v163
	v_add_f32_e32 v160, v160, v162
	v_add_f32_e32 v161, v161, v163
	v_mov_b32_e32 v144, v160
	v_mov_b32_e32 v145, v161
	s_nop 1
	v_permlane32_swap_b32_e32 v160, v144
	v_permlane32_swap_b32_e32 v161, v145
	v_add_f32_e32 v160, v160, v144
	v_add_f32_e32 v161, v161, v145
	v_cvt_pk_f16_f32 v137, v160, v161
	s_and_saveexec_b64 s[4:5], vcc
	global_atomic_pk_add_f16 v136, v137, s[20:21]
	s_endpgm
	.p2align	8
